# speedup vs baseline: 1.0005x; 1.0005x over previous
.Lmk_p72:
	v_mov_b32_e32 v175, v176
	v_mov_b32_e32 v198, v183
	v_lshrrev_b32_e32 v34, 3, v110
	v_add_u32_e32 v34, s33, v34
	v_lshl_or_b32 v34, v34, 7, v175
	global_load_dwordx4 v[176:179], v34, s[28:29]
	v_add_u32_e32 v36, 0x400, v34
	global_load_dwordx4 v[180:183], v36, s[28:29]
	v_bfe_u32 v121, v121, 16, 4
	v_mov_b64_e32 v[130:131], 0
	v_mov_b64_e32 v[132:133], 0
	v_mov_b64_e32 v[134:135], 0
	v_mov_b64_e32 v[136:137], 0
	v_mov_b64_e32 v[138:139], 0
	v_mov_b64_e32 v[140:141], 0
	v_mov_b64_e32 v[142:143], 0
	v_mov_b64_e32 v[144:145], 0
	v_and_b32_e32 v200, 1, v114
	v_cmp_eq_u32_e32 vcc, 1, v200
	s_nop 1
	v_cndmask_b32_e32 v124, v124, v174, vcc
	v_mov_b64_e32 v[168:169], s[12:13]
	v_mov_b64_e32 v[170:171], s[12:13]
	v_xor_b32_e32 v117, 64, v122
	s_mov_b32 s30, s85
	s_lshl_b32 s6, s43, 6
	s_sub_i32 s83, s44, s6
	s_lshl_b32 s6, s43, 8
	s_add_i32 s82, s78, s6
	s_mov_b32 s66, s41
	s_branch .LBB2_62

.Lmk_half_join:
	v_add_f32_e32 v34, v34, v121
	v_mul_f32_e32 v121, 0x3e4ccccd, v34
	v_max_f32_e32 v34, v34, v121
	v_cmp_gt_f32_e32 vcc, v34, v184
	s_and_b64 s[68:69], s[56:57], vcc
	s_cmp_eq_u64 s[68:69], 0
	s_cbranch_scc0 .Lmk_max
	v_add_u32_e32 v229, s82, v172
	v_add_u32_e32 v230, s82, v173
	ds_read_u16 v224, v229 offset:0
	ds_read_u16 v225, v229 offset:32
	ds_read_u16 v226, v229 offset:64
	ds_read_u16 v227, v229 offset:96
	ds_read_u16 v232, v229 offset:128
	ds_read_u16 v233, v229 offset:160
	ds_read_u16 v234, v229 offset:192
	ds_read_u16 v235, v229 offset:224
	v_bfe_u32 v121, v198, 16, 4
	ds_read_b32 v198, v230

.LBB2_110:
.Lmk_gather:
	s_mov_b32 s30, s83
	s_cmp_eq_u32 s43, 0
	s_cbranch_scc1 .Lmk_gather_first
	v_lshl_or_b32 v10, v224, 7, v175
	v_lshl_or_b32 v14, v225, 7, v175
	s_cmp_lt_i32 s83, 17
	global_load_dwordx4 v[10:13], v10, s[28:29]
	global_load_dwordx4 v[14:17], v14, s[28:29]
	s_cbranch_scc1 .LBB2_68
.Lmk_gather_p2:
	v_lshl_or_b32 v30, v226, 7, v175
	v_lshl_or_b32 v26, v227, 7, v175
	s_cmp_lt_i32 s83, 33
	global_load_dwordx4 v[30:33], v30, s[28:29]
	global_load_dwordx4 v[26:29], v26, s[28:29]
	s_cbranch_scc1 .LBB2_68
	v_lshl_or_b32 v2, v232, 7, v175
	v_lshl_or_b32 v6, v233, 7, v175
	v_lshl_or_b32 v18, v234, 7, v175
	v_lshl_or_b32 v22, v235, 7, v175
	global_load_dwordx4 v[2:5], v2, s[28:29]
	global_load_dwordx4 v[6:9], v6, s[28:29]
	global_load_dwordx4 v[18:21], v18, s[28:29]
	global_load_dwordx4 v[22:25], v22, s[28:29]

.LBB2_72:
.LBB2_74:
	s_add_i32 s34, s45, -1
	s_cmp_lg_u32 s49, s34
	s_cbranch_scc1 .Lmk_tail
	s_and_b64 vcc, exec, s[54:55]
	s_cbranch_vccz .Lmk_ma_ready
	s_waitcnt vmcnt(0)

.Lmk_max:
	v_cndmask_b32_e64 v161, v185, v34, s[56:57]
	s_nop 1
	v_max_f32_dpp v161, v161, v161 row_shr:1 row_mask:0xf bank_mask:0xf
	v_bfe_u32 v121, v198, 16, 4
	s_nop 0
	v_max_f32_dpp v161, v161, v161 row_shr:2 row_mask:0xf bank_mask:0xf
	v_add_u32_e32 v229, s82, v172
	v_add_u32_e32 v230, s82, v173
	v_max_f32_dpp v161, v161, v161 row_shr:4 row_mask:0xf bank_mask:0xf
	ds_read_u16 v224, v229 offset:0
	ds_read_u16 v225, v229 offset:32
	v_max_f32_dpp v161, v161, v161 row_shr:8 row_mask:0xf bank_mask:0xf
	ds_read_u16 v226, v229 offset:64
	ds_read_u16 v227, v229 offset:96
	v_max_f32_dpp v161, v161, v161 row_bcast:15 row_mask:0xa bank_mask:0xf
	ds_read_u16 v232, v229 offset:128
	ds_read_u16 v233, v229 offset:160
	v_max_f32_dpp v161, v161, v161 row_bcast:31 row_mask:0xc bank_mask:0xf
	ds_read_u16 v234, v229 offset:192
	ds_read_u16 v235, v229 offset:224
	v_readlane_b32 s70, v161, 63
	ds_read_b32 v198, v230
	s_and_b64 vcc, exec, s[54:55]
	s_nop 0
	v_mov_b32_e32 v161, s70
	s_cbranch_vccz .Lmk_rescale

.Lmk_gather_first:
	v_mov_b64_e32 v[10:11], v[176:177]
	v_mov_b64_e32 v[12:13], v[178:179]
	v_mov_b64_e32 v[14:15], v[180:181]
	v_mov_b64_e32 v[16:17], v[182:183]
	s_cmp_lt_i32 s83, 17
	s_cbranch_scc1 .LBB2_68
	s_branch .Lmk_gather_p2

.Lmk_reread:
	v_add_u32_e32 v229, s82, v172
	v_add_u32_e32 v230, s82, v173
	ds_read_u16 v224, v229 offset:0
	ds_read_u16 v225, v229 offset:32
	ds_read_u16 v226, v229 offset:64
	ds_read_u16 v227, v229 offset:96
	ds_read_u16 v232, v229 offset:128
	ds_read_u16 v233, v229 offset:160
	ds_read_u16 v234, v229 offset:192
	ds_read_u16 v235, v229 offset:224
	ds_read_b32 v198, v230
	s_waitcnt lgkmcnt(0)
	s_branch .Lmk_gather
